# baseline (speedup 1.0000x reference)
_Z5k_decPKiPKDF16_S2_PKfS4_S4_Pf:
	s_load_dword s3, s[0:1], 0x44
	s_load_dword s6, s[0:1], 0x38
	s_load_dwordx2 s[4:5], s[0:1], 0x0
	s_load_dwordx8 s[28:35], s[0:1], 0x8
	s_load_dwordx4 s[12:15], s[0:1], 0x28
	v_and_b32_e32 v1, 15, v0
	v_and_b32_e32 v64, 63, v0
	v_lshlrev_b32_e32 v96, 3, v1
	v_lshrrev_b32_e32 v4, 3, v0
	v_and_b32_e32 v4, 4, v4
	v_or_b32_e32 v96, v96, v4
	v_mov_b32_e32 v97, 0
	v_and_b32_e32 v104, 16, v0
	v_lshlrev_b32_e32 v6, 7, v0
	v_lshlrev_b32_e32 v7, 2, v64
	s_movk_i32 s16, 0x6000
	v_and_or_b32 v103, v6, s16, v7
	v_mov_b32_e32 v219, 0
	s_movk_i32 s19, 0x3d08
	s_waitcnt lgkmcnt(0)
	s_and_b32 s3, s3, 0xffff
	s_mul_i32 s2, s2, s3
	v_add_u32_e32 v5, s2, v0
	s_mul_i32 s6, s6, s3
	v_lshrrev_b32_e32 v102, 6, v5
	s_lshr_b32 s18, s6, 6
	v_readfirstlane_b32 s23, v102
	v_lshl_add_u64 v[2:3], s[4:5], 0, v[96:97]
	s_mov_b32 s16, 0xf4240
	v_cmp_gt_u32_e32 vcc, s16, v5
	s_and_saveexec_b64 s[22:23], vcc
	s_cbranch_execz .LBB2_3
	v_mov_b32_e32 v222, v2
	v_mov_b32_e32 v223, v3
	v_min_u32_e32 v218, s19, v102
	v_lshlrev_b32_e32 v218, 9, v218
	v_lshl_add_u64 v[216:217], v[222:223], 0, v[218:219]
	global_load_dword v65, v[216:217], off nt
	global_load_dword v80, v[216:217], off offset:128 nt
	global_load_dword v81, v[216:217], off offset:256 nt
	global_load_dword v82, v[216:217], off offset:384 nt
	v_add_u32_e32 v220, s18, v102
	v_min_u32_e32 v218, s19, v220
	v_lshlrev_b32_e32 v218, 9, v218
	v_lshl_add_u64 v[216:217], v[222:223], 0, v[218:219]
	global_load_dword v100, v[216:217], off nt
	global_load_dword v101, v[216:217], off offset:128 nt
	global_load_dword v98, v[216:217], off offset:256 nt
	global_load_dword v99, v[216:217], off offset:384 nt
	s_mov_b32 s8, s28
	s_and_b32 s9, s29, 0xffff
	s_mov_b32 s10, 0x30d400
	s_mov_b32 s11, 0x20000
	s_mov_b64 s[36:37], 0x1000
	v_and_b32_e32 v96, 48, v64
	v_lshlrev_b32_e32 v221, 6, v1
	v_lshlrev_b32_e32 v211, 2, v1
	v_lshlrev_b32_e32 v214, 4, v0
	v_add_u32_e32 v215, 0x1000, v214
	v_lshl_add_u32 v134, v1, 6, v96
	v_add_u32_e32 v134, 0x9000, v134
	v_readfirstlane_b32 s40, v0
	s_lshr_b32 s40, s40, 6
	s_lshl_b32 s40, s40, 10
	s_add_u32 s40, s40, 0x9000
	v_lshl_or_b32 v221, v102, 6, v64
	v_lshrrev_b32_e32 v213, 4, v64
	v_cmp_gt_u32_e32 vcc, 16, v64
	v_and_b32_e32 v210, 31, v64
	v_lshlrev_b32_e32 v210, 4, v210
	s_mov_b32 s38, -1
	s_mov_b32 s39, 0
	s_mov_b64 exec, s[38:39]
	global_load_dwordx4 v[126:129], v210, s[32:33]
	s_mov_b32 s38, 0
	s_mov_b32 s39, -1
	s_mov_b64 exec, s[38:39]
	global_load_dwordx4 v[126:129], v210, s[34:35]
	s_mov_b64 exec, -1
	s_mov_b32 m0, s40
	s_add_u32 s40, s40, 0x1000
	global_load_lds_dwordx4 v214, s[30:31]
	s_mov_b32 m0, s40
	s_nop 0
	global_load_lds_dwordx4 v215, s[30:31]
	s_load_dword s12, s[12:13], 0x0
	s_waitcnt vmcnt(8)
	v_lshl_or_b32 v216, v65, 5, v104
	v_lshl_or_b32 v217, v80, 5, v104
	v_lshl_or_b32 v218, v81, 5, v104
	v_lshl_or_b32 v212, v82, 5, v104
	buffer_load_dwordx4 v[92:95], v216, s[8:11], 0 offen
	buffer_load_dwordx4 v[88:91], v217, s[8:11], 0 offen
	buffer_load_dwordx4 v[84:87], v218, s[8:11], 0 offen
	buffer_load_dwordx4 v[80:83], v212, s[8:11], 0 offen
	s_lshl_b32 s21, s18, 6
	s_mov_b32 s20, 2
	s_mov_b64 s[16:17], 0
	v_cmp_eq_u32_e64 s[0:1], 1, v213
	v_cmp_eq_u32_e64 s[2:3], 2, v213
	v_cmp_eq_u32_e64 s[4:5], 3, v213
	v_mov_b32_e32 v96, v221
	v_mov_b32_e32 v97, 0
	s_waitcnt vmcnt(4)
	v_lshrrev_b32_e32 v210, 6, v0
	v_lshlrev_b32_e32 v210, 10, v210
	v_add_u32_e32 v210, 0x8000, v210
	v_lshl_add_u32 v130, v64, 4, v210
	v_lshl_add_u32 v131, v213, 4, v210
	v_add_u32_e32 v132, v211, v210
	ds_write_b128 v130, v[126:129]
	ds_read_b128 v[68:71], v131 offset:512
	ds_read_b128 v[72:75], v131 offset:576
	ds_read_b128 v[76:79], v131 offset:640
	ds_read_b128 v[106:109], v131 offset:704
	ds_read_b128 v[110:113], v131 offset:768
	ds_read_b128 v[114:117], v131 offset:832
	ds_read_b128 v[118:121], v131 offset:896
	ds_read_b128 v[122:125], v131 offset:960
	s_waitcnt lgkmcnt(0)
	ds_read_b32 v148, v132 offset:512
	ds_read_b32 v149, v132 offset:576
	ds_read_b32 v150, v132 offset:640
	ds_read_b32 v151, v132 offset:704
	ds_read_b32 v152, v132 offset:768
	ds_read_b32 v153, v132 offset:832
	ds_read_b32 v154, v132 offset:896
	ds_read_b32 v155, v132 offset:960
	ds_read_b32 v156, v132 offset:0
	ds_read_b32 v157, v132 offset:64
	ds_read_b32 v158, v132 offset:128
	ds_read_b32 v159, v132 offset:192
	s_waitcnt lgkmcnt(0)
	ds_read_b32 v160, v132 offset:256
	ds_read_b32 v161, v132 offset:320
	ds_read_b32 v162, v132 offset:384
	ds_read_b32 v163, v132 offset:448
	ds_read_b128 v[0:3], v131 offset:0
	ds_read_b128 v[4:7], v131 offset:64
	ds_read_b128 v[8:11], v131 offset:128
	ds_read_b128 v[12:15], v131 offset:192
	ds_read_b128 v[16:19], v131 offset:256
	ds_read_b128 v[20:23], v131 offset:320
	ds_read_b128 v[24:27], v131 offset:384
	ds_read_b128 v[28:31], v131 offset:448
	s_waitcnt lgkmcnt(0)
	s_barrier
	ds_read_b128 v[32:35], v134
	ds_read_b128 v[36:39], v134 offset:1024
	ds_read_b128 v[40:43], v134 offset:2048
	ds_read_b128 v[44:47], v134 offset:3072
	ds_read_b128 v[48:51], v134 offset:4096
	ds_read_b128 v[52:55], v134 offset:5120
	ds_read_b128 v[56:59], v134 offset:6144
	ds_read_b128 v[60:63], v134 offset:7168
	v_cvt_pk_f16_f32 v67, v74, v75
	v_cvt_pk_f16_f32 v66, v72, v73
	v_cvt_pk_f16_f32 v65, v70, v71
	v_cvt_pk_f16_f32 v64, v68, v69
	v_cvt_pk_f16_f32 v71, v108, v109
	v_cvt_pk_f16_f32 v70, v106, v107
	v_cvt_pk_f16_f32 v69, v78, v79
	v_cvt_pk_f16_f32 v68, v76, v77
	v_cvt_pk_f16_f32 v75, v116, v117
	v_cvt_pk_f16_f32 v74, v114, v115
	v_cvt_pk_f16_f32 v73, v112, v113
	v_cvt_pk_f16_f32 v72, v110, v111
	v_cvt_pk_f16_f32 v79, v124, v125
	v_cvt_pk_f16_f32 v78, v122, v123
	v_cvt_pk_f16_f32 v77, v120, v121
	v_cvt_pk_f16_f32 v76, v118, v119
	v_mov_b32_e32 v167, 0x38003800
	v_pk_mul_f16 v64, v64, v167
	v_pk_mul_f16 v65, v65, v167
	v_pk_mul_f16 v66, v66, v167
	v_pk_mul_f16 v67, v67, v167
	v_pk_mul_f16 v68, v68, v167
	v_pk_mul_f16 v69, v69, v167
	v_pk_mul_f16 v70, v70, v167
	v_pk_mul_f16 v71, v71, v167
	v_pk_mul_f16 v72, v72, v167
	v_pk_mul_f16 v73, v73, v167
	v_pk_mul_f16 v74, v74, v167
	v_pk_mul_f16 v75, v75, v167
	v_pk_mul_f16 v76, v76, v167
	v_pk_mul_f16 v77, v77, v167
	v_pk_mul_f16 v78, v78, v167
	v_pk_mul_f16 v79, v79, v167
	v_cvt_f16_f32_e32 v148, v148
	v_cvt_f16_f32_e32 v149, v149
	v_cvt_f16_f32_e32 v150, v150
	v_cvt_f16_f32_e32 v151, v151
	v_cvt_f16_f32_e32 v152, v152
	v_cvt_f16_f32_e32 v153, v153
	v_cvt_f16_f32_e32 v154, v154
	v_cvt_f16_f32_e32 v155, v155
	v_cvt_f32_f16_e32 v148, v148
	v_cvt_f32_f16_e32 v149, v149
	v_cvt_f32_f16_e32 v150, v150
	v_cvt_f32_f16_e32 v151, v151
	v_cvt_f32_f16_e32 v152, v152
	v_cvt_f32_f16_e32 v153, v153
	v_cvt_f32_f16_e32 v154, v154
	v_cvt_f32_f16_e32 v155, v155
	v_mul_f32_e32 v148, 0.5, v148
	v_mul_f32_e32 v149, 0.5, v149
	v_mul_f32_e32 v150, 0.5, v150
	v_mul_f32_e32 v151, 0.5, v151
	v_mul_f32_e32 v152, 0.5, v152
	v_mul_f32_e32 v153, 0.5, v153
	v_mul_f32_e32 v154, 0.5, v154
	v_mul_f32_e32 v155, 0.5, v155
	v_mov_b32_e32 v140, 0
	v_mov_b32_e32 v141, 0
	v_mov_b32_e32 v142, 0
	v_mov_b32_e32 v143, 0
	v_mov_b32_e32 v144, 0
	v_mov_b32_e32 v145, 0
	v_mov_b32_e32 v146, 0
	v_mov_b32_e32 v147, 0
	v_mov_b32_e32 v166, 0
	s_waitcnt lgkmcnt(0)
	v_cvt_f32_f16_e32 v164, v32
	v_cvt_f32_f16_sdwa v165, v32 dst_sel:DWORD dst_unused:UNUSED_PAD src0_sel:WORD_1
	v_fmac_f32_e32 v140, v148, v164
	v_fmac_f32_e32 v141, v148, v165
	v_cvt_f32_f16_e32 v164, v33
	v_cvt_f32_f16_sdwa v165, v33 dst_sel:DWORD dst_unused:UNUSED_PAD src0_sel:WORD_1
	v_fmac_f32_e32 v142, v148, v164
	v_fmac_f32_e32 v143, v148, v165
	v_cvt_f32_f16_e32 v164, v34
	v_cvt_f32_f16_sdwa v165, v34 dst_sel:DWORD dst_unused:UNUSED_PAD src0_sel:WORD_1
	v_fmac_f32_e32 v144, v148, v164
	v_fmac_f32_e32 v145, v148, v165
	v_cvt_f32_f16_e32 v164, v35
	v_cvt_f32_f16_sdwa v165, v35 dst_sel:DWORD dst_unused:UNUSED_PAD src0_sel:WORD_1
	v_fmac_f32_e32 v146, v148, v164
	v_fmac_f32_e32 v147, v148, v165
	v_fmac_f32_e32 v166, v148, v156
	v_cvt_f32_f16_e32 v164, v36
	v_cvt_f32_f16_sdwa v165, v36 dst_sel:DWORD dst_unused:UNUSED_PAD src0_sel:WORD_1
	v_fmac_f32_e32 v140, v149, v164
	v_fmac_f32_e32 v141, v149, v165
	v_cvt_f32_f16_e32 v164, v37
	v_cvt_f32_f16_sdwa v165, v37 dst_sel:DWORD dst_unused:UNUSED_PAD src0_sel:WORD_1
	v_fmac_f32_e32 v142, v149, v164
	v_fmac_f32_e32 v143, v149, v165
	v_cvt_f32_f16_e32 v164, v38
	v_cvt_f32_f16_sdwa v165, v38 dst_sel:DWORD dst_unused:UNUSED_PAD src0_sel:WORD_1
	v_fmac_f32_e32 v144, v149, v164
	v_fmac_f32_e32 v145, v149, v165
	v_cvt_f32_f16_e32 v164, v39
	v_cvt_f32_f16_sdwa v165, v39 dst_sel:DWORD dst_unused:UNUSED_PAD src0_sel:WORD_1
	v_fmac_f32_e32 v146, v149, v164
	v_fmac_f32_e32 v147, v149, v165
	v_fmac_f32_e32 v166, v149, v157
	v_cvt_f32_f16_e32 v164, v40
	v_cvt_f32_f16_sdwa v165, v40 dst_sel:DWORD dst_unused:UNUSED_PAD src0_sel:WORD_1
	v_fmac_f32_e32 v140, v150, v164
	v_fmac_f32_e32 v141, v150, v165
	v_cvt_f32_f16_e32 v164, v41
	v_cvt_f32_f16_sdwa v165, v41 dst_sel:DWORD dst_unused:UNUSED_PAD src0_sel:WORD_1
	v_fmac_f32_e32 v142, v150, v164
	v_fmac_f32_e32 v143, v150, v165
	v_cvt_f32_f16_e32 v164, v42
	v_cvt_f32_f16_sdwa v165, v42 dst_sel:DWORD dst_unused:UNUSED_PAD src0_sel:WORD_1
	v_fmac_f32_e32 v144, v150, v164
	v_fmac_f32_e32 v145, v150, v165
	v_cvt_f32_f16_e32 v164, v43
	v_cvt_f32_f16_sdwa v165, v43 dst_sel:DWORD dst_unused:UNUSED_PAD src0_sel:WORD_1
	v_fmac_f32_e32 v146, v150, v164
	v_fmac_f32_e32 v147, v150, v165
	v_fmac_f32_e32 v166, v150, v158
	v_cvt_f32_f16_e32 v164, v44
	v_cvt_f32_f16_sdwa v165, v44 dst_sel:DWORD dst_unused:UNUSED_PAD src0_sel:WORD_1
	v_fmac_f32_e32 v140, v151, v164
	v_fmac_f32_e32 v141, v151, v165
	v_cvt_f32_f16_e32 v164, v45
	v_cvt_f32_f16_sdwa v165, v45 dst_sel:DWORD dst_unused:UNUSED_PAD src0_sel:WORD_1
	v_fmac_f32_e32 v142, v151, v164
	v_fmac_f32_e32 v143, v151, v165
	v_cvt_f32_f16_e32 v164, v46
	v_cvt_f32_f16_sdwa v165, v46 dst_sel:DWORD dst_unused:UNUSED_PAD src0_sel:WORD_1
	v_fmac_f32_e32 v144, v151, v164
	v_fmac_f32_e32 v145, v151, v165
	v_cvt_f32_f16_e32 v164, v47
	v_cvt_f32_f16_sdwa v165, v47 dst_sel:DWORD dst_unused:UNUSED_PAD src0_sel:WORD_1
	v_fmac_f32_e32 v146, v151, v164
	v_fmac_f32_e32 v147, v151, v165
	v_fmac_f32_e32 v166, v151, v159
	v_cvt_f32_f16_e32 v164, v48
	v_cvt_f32_f16_sdwa v165, v48 dst_sel:DWORD dst_unused:UNUSED_PAD src0_sel:WORD_1
	v_fmac_f32_e32 v140, v152, v164
	v_fmac_f32_e32 v141, v152, v165
	v_cvt_f32_f16_e32 v164, v49
	v_cvt_f32_f16_sdwa v165, v49 dst_sel:DWORD dst_unused:UNUSED_PAD src0_sel:WORD_1
	v_fmac_f32_e32 v142, v152, v164
	v_fmac_f32_e32 v143, v152, v165
	v_cvt_f32_f16_e32 v164, v50
	v_cvt_f32_f16_sdwa v165, v50 dst_sel:DWORD dst_unused:UNUSED_PAD src0_sel:WORD_1
	v_fmac_f32_e32 v144, v152, v164
	v_fmac_f32_e32 v145, v152, v165
	v_cvt_f32_f16_e32 v164, v51
	v_cvt_f32_f16_sdwa v165, v51 dst_sel:DWORD dst_unused:UNUSED_PAD src0_sel:WORD_1
	v_fmac_f32_e32 v146, v152, v164
	v_fmac_f32_e32 v147, v152, v165
	v_fmac_f32_e32 v166, v152, v160
	v_cvt_f32_f16_e32 v164, v52
	v_cvt_f32_f16_sdwa v165, v52 dst_sel:DWORD dst_unused:UNUSED_PAD src0_sel:WORD_1
	v_fmac_f32_e32 v140, v153, v164
	v_fmac_f32_e32 v141, v153, v165
	v_cvt_f32_f16_e32 v164, v53
	v_cvt_f32_f16_sdwa v165, v53 dst_sel:DWORD dst_unused:UNUSED_PAD src0_sel:WORD_1
	v_fmac_f32_e32 v142, v153, v164
	v_fmac_f32_e32 v143, v153, v165
	v_cvt_f32_f16_e32 v164, v54
	v_cvt_f32_f16_sdwa v165, v54 dst_sel:DWORD dst_unused:UNUSED_PAD src0_sel:WORD_1
	v_fmac_f32_e32 v144, v153, v164
	v_fmac_f32_e32 v145, v153, v165
	v_cvt_f32_f16_e32 v164, v55
	v_cvt_f32_f16_sdwa v165, v55 dst_sel:DWORD dst_unused:UNUSED_PAD src0_sel:WORD_1
	v_fmac_f32_e32 v146, v153, v164
	v_fmac_f32_e32 v147, v153, v165
	v_fmac_f32_e32 v166, v153, v161
	v_cvt_f32_f16_e32 v164, v56
	v_cvt_f32_f16_sdwa v165, v56 dst_sel:DWORD dst_unused:UNUSED_PAD src0_sel:WORD_1
	v_fmac_f32_e32 v140, v154, v164
	v_fmac_f32_e32 v141, v154, v165
	v_cvt_f32_f16_e32 v164, v57
	v_cvt_f32_f16_sdwa v165, v57 dst_sel:DWORD dst_unused:UNUSED_PAD src0_sel:WORD_1
	v_fmac_f32_e32 v142, v154, v164
	v_fmac_f32_e32 v143, v154, v165
	v_cvt_f32_f16_e32 v164, v58
	v_cvt_f32_f16_sdwa v165, v58 dst_sel:DWORD dst_unused:UNUSED_PAD src0_sel:WORD_1
	v_fmac_f32_e32 v144, v154, v164
	v_fmac_f32_e32 v145, v154, v165
	v_cvt_f32_f16_e32 v164, v59
	v_cvt_f32_f16_sdwa v165, v59 dst_sel:DWORD dst_unused:UNUSED_PAD src0_sel:WORD_1
	v_fmac_f32_e32 v146, v154, v164
	v_fmac_f32_e32 v147, v154, v165
	v_fmac_f32_e32 v166, v154, v162
	v_cvt_f32_f16_e32 v164, v60
	v_cvt_f32_f16_sdwa v165, v60 dst_sel:DWORD dst_unused:UNUSED_PAD src0_sel:WORD_1
	v_fmac_f32_e32 v140, v155, v164
	v_fmac_f32_e32 v141, v155, v165
	v_cvt_f32_f16_e32 v164, v61
	v_cvt_f32_f16_sdwa v165, v61 dst_sel:DWORD dst_unused:UNUSED_PAD src0_sel:WORD_1
	v_fmac_f32_e32 v142, v155, v164
	v_fmac_f32_e32 v143, v155, v165
	v_cvt_f32_f16_e32 v164, v62
	v_cvt_f32_f16_sdwa v165, v62 dst_sel:DWORD dst_unused:UNUSED_PAD src0_sel:WORD_1
	v_fmac_f32_e32 v144, v155, v164
	v_fmac_f32_e32 v145, v155, v165
	v_cvt_f32_f16_e32 v164, v63
	v_cvt_f32_f16_sdwa v165, v63 dst_sel:DWORD dst_unused:UNUSED_PAD src0_sel:WORD_1
	v_fmac_f32_e32 v146, v155, v164
	v_fmac_f32_e32 v147, v155, v165
	v_fmac_f32_e32 v166, v155, v163
	v_add_f32_dpp v140, v140, v140 row_ror:8 row_mask:0xf bank_mask:0xf
	v_add_f32_dpp v141, v141, v141 row_ror:8 row_mask:0xf bank_mask:0xf
	v_add_f32_dpp v142, v142, v142 row_ror:8 row_mask:0xf bank_mask:0xf
	v_add_f32_dpp v143, v143, v143 row_ror:8 row_mask:0xf bank_mask:0xf
	v_add_f32_dpp v144, v144, v144 row_ror:8 row_mask:0xf bank_mask:0xf
	v_add_f32_dpp v145, v145, v145 row_ror:8 row_mask:0xf bank_mask:0xf
	v_add_f32_dpp v146, v146, v146 row_ror:8 row_mask:0xf bank_mask:0xf
	v_add_f32_dpp v147, v147, v147 row_ror:8 row_mask:0xf bank_mask:0xf
	v_add_f32_dpp v166, v166, v166 row_ror:8 row_mask:0xf bank_mask:0xf
	v_add_f32_dpp v140, v140, v140 row_ror:4 row_mask:0xf bank_mask:0xf
	v_add_f32_dpp v141, v141, v141 row_ror:4 row_mask:0xf bank_mask:0xf
	v_add_f32_dpp v142, v142, v142 row_ror:4 row_mask:0xf bank_mask:0xf
	v_add_f32_dpp v143, v143, v143 row_ror:4 row_mask:0xf bank_mask:0xf
	v_add_f32_dpp v144, v144, v144 row_ror:4 row_mask:0xf bank_mask:0xf
	v_add_f32_dpp v145, v145, v145 row_ror:4 row_mask:0xf bank_mask:0xf
	v_add_f32_dpp v146, v146, v146 row_ror:4 row_mask:0xf bank_mask:0xf
	v_add_f32_dpp v147, v147, v147 row_ror:4 row_mask:0xf bank_mask:0xf
	v_add_f32_dpp v166, v166, v166 row_ror:4 row_mask:0xf bank_mask:0xf
	v_add_f32_dpp v140, v140, v140 row_ror:2 row_mask:0xf bank_mask:0xf
	v_add_f32_dpp v141, v141, v141 row_ror:2 row_mask:0xf bank_mask:0xf
	v_add_f32_dpp v142, v142, v142 row_ror:2 row_mask:0xf bank_mask:0xf
	v_add_f32_dpp v143, v143, v143 row_ror:2 row_mask:0xf bank_mask:0xf
	v_add_f32_dpp v144, v144, v144 row_ror:2 row_mask:0xf bank_mask:0xf
	v_add_f32_dpp v145, v145, v145 row_ror:2 row_mask:0xf bank_mask:0xf
	v_add_f32_dpp v146, v146, v146 row_ror:2 row_mask:0xf bank_mask:0xf
	v_add_f32_dpp v147, v147, v147 row_ror:2 row_mask:0xf bank_mask:0xf
	v_add_f32_dpp v166, v166, v166 row_ror:2 row_mask:0xf bank_mask:0xf
	v_add_f32_dpp v140, v140, v140 row_ror:1 row_mask:0xf bank_mask:0xf
	v_add_f32_dpp v141, v141, v141 row_ror:1 row_mask:0xf bank_mask:0xf
	v_add_f32_dpp v142, v142, v142 row_ror:1 row_mask:0xf bank_mask:0xf
	v_add_f32_dpp v143, v143, v143 row_ror:1 row_mask:0xf bank_mask:0xf
	v_add_f32_dpp v144, v144, v144 row_ror:1 row_mask:0xf bank_mask:0xf
	v_add_f32_dpp v145, v145, v145 row_ror:1 row_mask:0xf bank_mask:0xf
	v_add_f32_dpp v146, v146, v146 row_ror:1 row_mask:0xf bank_mask:0xf
	v_add_f32_dpp v147, v147, v147 row_ror:1 row_mask:0xf bank_mask:0xf
	v_add_f32_dpp v166, v166, v166 row_ror:1 row_mask:0xf bank_mask:0xf
	v_cvt_pk_f16_f32 v252, v140, v141
	v_cvt_pk_f16_f32 v253, v142, v143
	v_cvt_pk_f16_f32 v254, v144, v145
	v_cvt_pk_f16_f32 v255, v146, v147
	s_waitcnt lgkmcnt(0)
	v_add_f32_e32 v209, s12, v166
	v_add_u32_e32 v220, s18, v102
	v_add_u32_e32 v220, s18, v220
	v_min_u32_e32 v218, s19, v220
	v_lshlrev_b32_e32 v218, 9, v218
	v_lshl_add_u64 v[216:217], v[222:223], 0, v[218:219]
	global_load_dword v228, v[216:217], off nt
	global_load_dword v229, v[216:217], off offset:128 nt
	global_load_dword v230, v[216:217], off offset:256 nt
	global_load_dword v231, v[216:217], off offset:384 nt
	v_add_u32_e32 v220, s18, v220
	v_min_u32_e32 v218, s19, v220
	v_lshlrev_b32_e32 v218, 9, v218
	v_lshl_add_u64 v[216:217], v[222:223], 0, v[218:219]
	global_load_dword v232, v[216:217], off nt
	global_load_dword v233, v[216:217], off offset:128 nt
	global_load_dword v234, v[216:217], off offset:256 nt
	global_load_dword v235, v[216:217], off offset:384 nt
	v_add_u32_e32 v220, s18, v220
	v_min_u32_e32 v218, s19, v220
	v_lshlrev_b32_e32 v218, 9, v218
	v_lshl_add_u64 v[216:217], v[222:223], 0, v[218:219]
	global_load_dword v236, v[216:217], off nt
	global_load_dword v237, v[216:217], off offset:128 nt
	global_load_dword v238, v[216:217], off offset:256 nt
	global_load_dword v239, v[216:217], off offset:384 nt
	v_add_u32_e32 v220, s18, v220
	v_min_u32_e32 v218, s19, v220
	v_lshlrev_b32_e32 v218, 9, v218
	v_lshl_add_u64 v[216:217], v[222:223], 0, v[218:219]
	global_load_dword v240, v[216:217], off nt
	global_load_dword v241, v[216:217], off offset:128 nt
	global_load_dword v242, v[216:217], off offset:256 nt
	global_load_dword v243, v[216:217], off offset:384 nt
	v_add_u32_e32 v220, s18, v220
	v_min_u32_e32 v218, s19, v220
	v_lshlrev_b32_e32 v218, 9, v218
	v_lshl_add_u64 v[216:217], v[222:223], 0, v[218:219]
	global_load_dword v244, v[216:217], off nt
	global_load_dword v245, v[216:217], off offset:128 nt
	global_load_dword v246, v[216:217], off offset:256 nt
	global_load_dword v247, v[216:217], off offset:384 nt
	v_add_u32_e32 v220, s18, v220
	v_min_u32_e32 v218, s19, v220
	v_lshlrev_b32_e32 v218, 9, v218
	v_lshl_add_u64 v[216:217], v[222:223], 0, v[218:219]
	global_load_dword v248, v[216:217], off nt
	global_load_dword v249, v[216:217], off offset:128 nt
	global_load_dword v250, v[216:217], off offset:256 nt
	global_load_dword v251, v[216:217], off offset:384 nt
	s_waitcnt vmcnt(24)
